# v69 + conv tap loop doubled with exchanged weight register sets, carrying moves removed
# baseline (speedup 1.0000x reference)
; #define LAS __attribute__((address_space(3)))
; __device__ __forceinline__ void ph_convpool_fast(const Args& a, LAS unsigned char* lds) {
;     ...
; #pragma unroll 1
;         for (int r0 = 0; r0 < 36; r0 += 4) {
; #pragma unroll
;             for (int u = 0; u < 4; ++u) { const int r = r0 + u;
;                 if (r < 31) unpack8(*(const LAS u32x4*)(lds + CW_OFF + r * 1024 + ch * 2), wq[u]);
;                 else {
; #pragma unroll
;                     for (int c = 0; c < 8; ++c) wq[u][c] = 0.f; }
;                 float v[8]; unpack8(*(const LAS u32x4*)(lds + VT_OFF + (4 * wave + (r < 33 ? r : 33)) * 1024 + ch * 2), v);
; #pragma unroll
;                 for (int j = 0; j < 4; ++j)
; #pragma unroll
;                     for (int c = 0; c < 8; ++c) acc[j][c] += wq[(u - j) & 3][c] * v[c];
;             }
;         }
.LBB0_294:
	s_waitcnt lgkmcnt(2)
	v_lshlrev_b32_e32 v183, 16, v27
	v_lshlrev_b32_e32 v182, 16, v26
	v_and_b32_e32 v27, 0xffff0000, v27
	v_and_b32_e32 v26, 0xffff0000, v26
	v_pk_fma_f32 v[78:79], v[118:119], v[26:27], v[78:79]
	v_pk_fma_f32 v[70:71], v[88:89], v[26:27], v[70:71]
	v_pk_fma_f32 v[62:63], v[96:97], v[26:27], v[62:63]
	v_pk_fma_f32 v[26:27], v[106:107], v[26:27], v[54:55]
	v_lshlrev_b32_e32 v55, 16, v29
	v_lshlrev_b32_e32 v54, 16, v28
	v_and_b32_e32 v29, 0xffff0000, v29
	v_and_b32_e32 v28, 0xffff0000, v28
	v_pk_fma_f32 v[80:81], v[122:123], v[182:183], v[80:81]
	v_pk_fma_f32 v[72:73], v[94:95], v[182:183], v[72:73]
	v_pk_fma_f32 v[64:65], v[102:103], v[182:183], v[64:65]
	v_pk_fma_f32 v[56:57], v[120:121], v[182:183], v[56:57]
	v_pk_fma_f32 v[76:77], v[116:117], v[54:55], v[76:77]
	v_pk_fma_f32 v[68:69], v[84:85], v[54:55], v[68:69]
	v_pk_fma_f32 v[60:61], v[90:91], v[54:55], v[60:61]
	v_pk_fma_f32 v[16:17], v[98:99], v[54:55], v[16:17]
	v_pk_fma_f32 v[54:55], v[110:111], v[28:29], v[74:75]
	v_pk_fma_f32 v[66:67], v[82:83], v[28:29], v[66:67]
	v_pk_fma_f32 v[58:59], v[86:87], v[28:29], v[58:59]
	v_pk_fma_f32 v[12:13], v[92:93], v[28:29], v[12:13]
	s_waitcnt lgkmcnt(1)
	v_lshlrev_b32_e32 v29, 16, v31
	v_lshlrev_b32_e32 v28, 16, v30
	v_and_b32_e32 v31, 0xffff0000, v31
	v_and_b32_e32 v30, 0xffff0000, v30
	v_pk_fma_f32 v[74:75], v[100:101], v[28:29], v[80:81]
	v_pk_fma_f32 v[72:73], v[122:123], v[28:29], v[72:73]
	v_pk_fma_f32 v[64:65], v[94:95], v[28:29], v[64:65]
	v_pk_fma_f32 v[28:29], v[102:103], v[28:29], v[56:57]
	v_pk_fma_f32 v[56:57], v[104:105], v[30:31], v[78:79]
	v_pk_fma_f32 v[70:71], v[118:119], v[30:31], v[70:71]
	v_pk_fma_f32 v[62:63], v[88:89], v[30:31], v[62:63]
	v_pk_fma_f32 v[26:27], v[96:97], v[30:31], v[26:27]
	v_lshlrev_b32_e32 v31, 16, v33
	v_lshlrev_b32_e32 v30, 16, v32
	v_pk_fma_f32 v[76:77], v[108:109], v[30:31], v[76:77]
	v_pk_fma_f32 v[68:69], v[116:117], v[30:31], v[68:69]
	v_pk_fma_f32 v[60:61], v[84:85], v[30:31], v[60:61]
	v_pk_fma_f32 v[16:17], v[90:91], v[30:31], v[16:17]
	v_and_b32_e32 v31, 0xffff0000, v33
	v_and_b32_e32 v30, 0xffff0000, v32
	v_pk_fma_f32 v[32:33], v[114:115], v[30:31], v[54:55]
	v_pk_fma_f32 v[54:55], v[110:111], v[30:31], v[66:67]
	v_pk_fma_f32 v[58:59], v[82:83], v[30:31], v[58:59]
	v_pk_fma_f32 v[12:13], v[86:87], v[30:31], v[12:13]
	s_waitcnt lgkmcnt(0)
	v_lshlrev_b32_e32 v31, 16, v35
	v_lshlrev_b32_e32 v30, 16, v34
	v_pk_fma_f32 v[66:67], v[124:125], v[30:31], v[74:75]
	v_pk_fma_f32 v[72:73], v[100:101], v[30:31], v[72:73]
	v_pk_fma_f32 v[64:65], v[122:123], v[30:31], v[64:65]
	v_pk_fma_f32 v[30:31], v[94:95], v[30:31], v[28:29]
	v_and_b32_e32 v29, 0xffff0000, v35
	v_and_b32_e32 v28, 0xffff0000, v34
	v_pk_fma_f32 v[74:75], v[88:89], v[28:29], v[26:27]
	v_lshlrev_b32_e32 v27, 16, v37
	v_lshlrev_b32_e32 v26, 16, v36
	s_min_u32 s8, s2, 33
	v_pk_fma_f32 v[76:77], v[128:129], v[26:27], v[76:77]
	v_pk_fma_f32 v[68:69], v[108:109], v[26:27], v[68:69]
	v_pk_fma_f32 v[60:61], v[116:117], v[26:27], v[60:61]
	v_pk_fma_f32 v[16:17], v[84:85], v[26:27], v[16:17]
	v_lshl_add_u32 v26, s8, 10, v151
	v_pk_fma_f32 v[34:35], v[126:127], v[28:29], v[56:57]
	v_pk_fma_f32 v[70:71], v[104:105], v[28:29], v[70:71]
	v_pk_fma_f32 v[62:63], v[118:119], v[28:29], v[62:63]
	ds_read_b128 v[26:29], v26
	v_and_b32_e32 v37, 0xffff0000, v37
	v_and_b32_e32 v36, 0xffff0000, v36
	v_pk_fma_f32 v[32:33], v[112:113], v[36:37], v[32:33]
	v_pk_fma_f32 v[84:85], v[114:115], v[36:37], v[54:55]
	v_pk_fma_f32 v[58:59], v[110:111], v[36:37], v[58:59]
	v_pk_fma_f32 v[12:13], v[82:83], v[36:37], v[12:13]
	s_waitcnt lgkmcnt(0)
	v_lshlrev_b32_e32 v37, 16, v27
	v_lshlrev_b32_e32 v36, 16, v26
	v_and_b32_e32 v27, 0xffff0000, v27
	v_and_b32_e32 v26, 0xffff0000, v26
	v_pk_fma_f32 v[78:79], v[132:133], v[26:27], v[34:35]
	v_pk_fma_f32 v[70:71], v[126:127], v[26:27], v[70:71]
	v_pk_fma_f32 v[62:63], v[104:105], v[26:27], v[62:63]
	v_pk_fma_f32 v[54:55], v[118:119], v[26:27], v[74:75]
	v_lshlrev_b32_e32 v27, 16, v29
	v_lshlrev_b32_e32 v26, 16, v28
	v_pk_fma_f32 v[76:77], v[134:135], v[26:27], v[76:77]
	v_pk_fma_f32 v[68:69], v[128:129], v[26:27], v[68:69]
	v_pk_fma_f32 v[60:61], v[108:109], v[26:27], v[60:61]
	v_pk_fma_f32 v[16:17], v[116:117], v[26:27], v[16:17]
	v_and_b32_e32 v27, 0xffff0000, v29
	v_and_b32_e32 v26, 0xffff0000, v28
	s_add_i32 s2, s2, 4
	v_pk_fma_f32 v[80:81], v[130:131], v[36:37], v[66:67]
	v_pk_fma_f32 v[72:73], v[124:125], v[36:37], v[72:73]
	v_pk_fma_f32 v[64:65], v[100:101], v[36:37], v[64:65]
	v_pk_fma_f32 v[56:57], v[122:123], v[36:37], v[30:31]
	v_pk_fma_f32 v[74:75], v[136:137], v[26:27], v[32:33]
	v_pk_fma_f32 v[66:67], v[112:113], v[26:27], v[84:85]
	v_pk_fma_f32 v[58:59], v[114:115], v[26:27], v[58:59]
	v_pk_fma_f32 v[12:13], v[110:111], v[26:27], v[12:13]
	v_add_u32_e32 v181, 0x1000, v181
	s_cmp_gt_u32 s3, 31
	s_cbranch_scc1 .LBB0_303
	s_branch .Lconv_b_295

; #define LAS __attribute__((address_space(3)))
; __device__ __forceinline__ void ph_convpool_fast(const Args& a, LAS unsigned char* lds) {
;     ...
; #pragma unroll 1
;         for (int r0 = 0; r0 < 36; r0 += 4) {
; #pragma unroll
;             for (int u = 0; u < 4; ++u) { const int r = r0 + u;
;                 if (r < 31) unpack8(*(const LAS u32x4*)(lds + CW_OFF + r * 1024 + ch * 2), wq[u]);
;                 else {
; #pragma unroll
;                     for (int c = 0; c < 8; ++c) wq[u][c] = 0.f; }
;                 float v[8]; unpack8(*(const LAS u32x4*)(lds + VT_OFF + (4 * wave + (r < 33 ? r : 33)) * 1024 + ch * 2), v);
; #pragma unroll
;                 for (int j = 0; j < 4; ++j)
; #pragma unroll
;                     for (int c = 0; c < 8; ++c) acc[j][c] += wq[(u - j) & 3][c] * v[c];
;             }
;         }
.Lconv_b_294:
	s_waitcnt lgkmcnt(2)
	v_lshlrev_b32_e32 v183, 16, v27
	v_lshlrev_b32_e32 v182, 16, v26
	v_and_b32_e32 v27, 0xffff0000, v27
	v_and_b32_e32 v26, 0xffff0000, v26
	v_pk_fma_f32 v[78:79], v[118:119], v[26:27], v[78:79]
	v_pk_fma_f32 v[70:71], v[132:133], v[26:27], v[70:71]
	v_pk_fma_f32 v[62:63], v[126:127], v[26:27], v[62:63]
	v_pk_fma_f32 v[26:27], v[104:105], v[26:27], v[54:55]
	v_lshlrev_b32_e32 v55, 16, v29
	v_lshlrev_b32_e32 v54, 16, v28
	v_and_b32_e32 v29, 0xffff0000, v29
	v_and_b32_e32 v28, 0xffff0000, v28
	v_pk_fma_f32 v[80:81], v[122:123], v[182:183], v[80:81]
	v_pk_fma_f32 v[72:73], v[130:131], v[182:183], v[72:73]
	v_pk_fma_f32 v[64:65], v[124:125], v[182:183], v[64:65]
	v_pk_fma_f32 v[56:57], v[100:101], v[182:183], v[56:57]
	v_pk_fma_f32 v[76:77], v[116:117], v[54:55], v[76:77]
	v_pk_fma_f32 v[68:69], v[134:135], v[54:55], v[68:69]
	v_pk_fma_f32 v[60:61], v[128:129], v[54:55], v[60:61]
	v_pk_fma_f32 v[16:17], v[108:109], v[54:55], v[16:17]
	v_pk_fma_f32 v[54:55], v[110:111], v[28:29], v[74:75]
	v_pk_fma_f32 v[66:67], v[136:137], v[28:29], v[66:67]
	v_pk_fma_f32 v[58:59], v[112:113], v[28:29], v[58:59]
	v_pk_fma_f32 v[12:13], v[114:115], v[28:29], v[12:13]
	s_waitcnt lgkmcnt(1)
	v_lshlrev_b32_e32 v29, 16, v31
	v_lshlrev_b32_e32 v28, 16, v30
	v_and_b32_e32 v31, 0xffff0000, v31
	v_and_b32_e32 v30, 0xffff0000, v30
	v_pk_fma_f32 v[74:75], v[120:121], v[28:29], v[80:81]
	v_pk_fma_f32 v[72:73], v[122:123], v[28:29], v[72:73]
	v_pk_fma_f32 v[64:65], v[130:131], v[28:29], v[64:65]
	v_pk_fma_f32 v[28:29], v[124:125], v[28:29], v[56:57]
	v_pk_fma_f32 v[56:57], v[106:107], v[30:31], v[78:79]
	v_pk_fma_f32 v[70:71], v[118:119], v[30:31], v[70:71]
	v_pk_fma_f32 v[62:63], v[132:133], v[30:31], v[62:63]
	v_pk_fma_f32 v[26:27], v[126:127], v[30:31], v[26:27]
	v_lshlrev_b32_e32 v31, 16, v33
	v_lshlrev_b32_e32 v30, 16, v32
	v_pk_fma_f32 v[76:77], v[98:99], v[30:31], v[76:77]
	v_pk_fma_f32 v[68:69], v[116:117], v[30:31], v[68:69]
	v_pk_fma_f32 v[60:61], v[134:135], v[30:31], v[60:61]
	v_pk_fma_f32 v[16:17], v[128:129], v[30:31], v[16:17]
	v_and_b32_e32 v31, 0xffff0000, v33
	v_and_b32_e32 v30, 0xffff0000, v32
	v_pk_fma_f32 v[32:33], v[92:93], v[30:31], v[54:55]
	v_pk_fma_f32 v[54:55], v[110:111], v[30:31], v[66:67]
	v_pk_fma_f32 v[58:59], v[136:137], v[30:31], v[58:59]
	v_pk_fma_f32 v[12:13], v[112:113], v[30:31], v[12:13]
	s_waitcnt lgkmcnt(0)
	v_lshlrev_b32_e32 v31, 16, v35
	v_lshlrev_b32_e32 v30, 16, v34
	v_pk_fma_f32 v[66:67], v[102:103], v[30:31], v[74:75]
	v_pk_fma_f32 v[72:73], v[120:121], v[30:31], v[72:73]
	v_pk_fma_f32 v[64:65], v[122:123], v[30:31], v[64:65]
	v_pk_fma_f32 v[30:31], v[130:131], v[30:31], v[28:29]
	v_and_b32_e32 v29, 0xffff0000, v35
	v_and_b32_e32 v28, 0xffff0000, v34
	v_pk_fma_f32 v[74:75], v[132:133], v[28:29], v[26:27]
	v_lshlrev_b32_e32 v27, 16, v37
	v_lshlrev_b32_e32 v26, 16, v36
	s_min_u32 s8, s2, 33
	v_pk_fma_f32 v[76:77], v[90:91], v[26:27], v[76:77]
	v_pk_fma_f32 v[68:69], v[98:99], v[26:27], v[68:69]
	v_pk_fma_f32 v[60:61], v[116:117], v[26:27], v[60:61]
	v_pk_fma_f32 v[16:17], v[134:135], v[26:27], v[16:17]
	v_lshl_add_u32 v26, s8, 10, v151
	v_pk_fma_f32 v[34:35], v[96:97], v[28:29], v[56:57]
	v_pk_fma_f32 v[70:71], v[106:107], v[28:29], v[70:71]
	v_pk_fma_f32 v[62:63], v[118:119], v[28:29], v[62:63]
	ds_read_b128 v[26:29], v26
	v_and_b32_e32 v37, 0xffff0000, v37
	v_and_b32_e32 v36, 0xffff0000, v36
	v_pk_fma_f32 v[32:33], v[86:87], v[36:37], v[32:33]
	v_pk_fma_f32 v[134:135], v[92:93], v[36:37], v[54:55]
	v_pk_fma_f32 v[58:59], v[110:111], v[36:37], v[58:59]
	v_pk_fma_f32 v[12:13], v[136:137], v[36:37], v[12:13]
	s_waitcnt lgkmcnt(0)
	v_lshlrev_b32_e32 v37, 16, v27
	v_lshlrev_b32_e32 v36, 16, v26
	v_and_b32_e32 v27, 0xffff0000, v27
	v_and_b32_e32 v26, 0xffff0000, v26
	v_pk_fma_f32 v[78:79], v[88:89], v[26:27], v[34:35]
	v_pk_fma_f32 v[70:71], v[96:97], v[26:27], v[70:71]
	v_pk_fma_f32 v[62:63], v[106:107], v[26:27], v[62:63]
	v_pk_fma_f32 v[54:55], v[118:119], v[26:27], v[74:75]
	v_lshlrev_b32_e32 v27, 16, v29
	v_lshlrev_b32_e32 v26, 16, v28
	v_pk_fma_f32 v[76:77], v[84:85], v[26:27], v[76:77]
	v_pk_fma_f32 v[68:69], v[90:91], v[26:27], v[68:69]
	v_pk_fma_f32 v[60:61], v[98:99], v[26:27], v[60:61]
	v_pk_fma_f32 v[16:17], v[116:117], v[26:27], v[16:17]
	v_and_b32_e32 v27, 0xffff0000, v29
	v_and_b32_e32 v26, 0xffff0000, v28
	s_add_i32 s2, s2, 4
	v_pk_fma_f32 v[80:81], v[94:95], v[36:37], v[66:67]
	v_pk_fma_f32 v[72:73], v[102:103], v[36:37], v[72:73]
	v_pk_fma_f32 v[64:65], v[120:121], v[36:37], v[64:65]
	v_pk_fma_f32 v[56:57], v[122:123], v[36:37], v[30:31]
	v_pk_fma_f32 v[74:75], v[82:83], v[26:27], v[32:33]
	v_pk_fma_f32 v[66:67], v[86:87], v[26:27], v[134:135]
	v_pk_fma_f32 v[58:59], v[92:93], v[26:27], v[58:59]
	v_pk_fma_f32 v[12:13], v[110:111], v[26:27], v[12:13]
	v_add_u32_e32 v181, 0x1000, v181
	s_cmp_gt_u32 s3, 31
	s_cbranch_scc1 .LBB0_303
	s_branch .LBB0_295

; #define LAS __attribute__((address_space(3)))
; __device__ __forceinline__ void ph_convpool_fast(const Args& a, LAS unsigned char* lds) {
;     ...
;             for (int u = 0; u < 4; ++u) { const int r = r0 + u;
;                 if (r < 31) unpack8(*(const LAS u32x4*)(lds + CW_OFF + r * 1024 + ch * 2), wq[u]);
;                 else {
; #pragma unroll
;                     for (int c = 0; c < 8; ++c) wq[u][c] = 0.f; }
;                 float v[8]; unpack8(*(const LAS u32x4*)(lds + VT_OFF + (4 * wave + (r < 33 ? r : 33)) * 1024 + ch * 2), v);
.Lconv_b_297:
	v_add_u32_e32 v30, v181, v140
	v_add_u32_e32 v26, 0xfffe4c00, v30
	ds_read_b128 v[26:29], v26
	s_add_i32 s8, s3, 1
	s_cmp_gt_u32 s8, 30
	s_cbranch_scc1 .Lconv_b_zero_w1
	ds_read_b128 v[32:35], v181 offset:1024
	s_waitcnt lgkmcnt(0)
	v_lshlrev_b32_e32 v120, 16, v32
	v_lshlrev_b32_e32 v121, 16, v33
	v_and_b32_e32 v107, 0xffff0000, v33
	v_and_b32_e32 v106, 0xffff0000, v32
	v_lshlrev_b32_e32 v98, 16, v34
	v_lshlrev_b32_e32 v99, 16, v35
	v_and_b32_e32 v93, 0xffff0000, v35
	v_and_b32_e32 v92, 0xffff0000, v34
.Lconv_b_299:
	v_add_u32_e32 v30, 0xfffe5000, v30
	ds_read_b128 v[30:33], v30
	s_add_i32 s8, s8, 1
	s_cmp_gt_u32 s8, 30
	s_cbranch_scc1 .Lconv_b_zero_w2
	ds_read_b128 v[34:37], v181 offset:2048
	s_waitcnt lgkmcnt(0)
	v_lshlrev_b32_e32 v102, 16, v34
	v_lshlrev_b32_e32 v103, 16, v35
	v_and_b32_e32 v97, 0xffff0000, v35
	v_and_b32_e32 v96, 0xffff0000, v34
	v_lshlrev_b32_e32 v90, 16, v36
	v_lshlrev_b32_e32 v91, 16, v37
	v_and_b32_e32 v87, 0xffff0000, v37
	v_and_b32_e32 v86, 0xffff0000, v36
.Lconv_b_301:
	s_add_i32 s8, s2, -1
	s_min_u32 s8, s8, 33
	v_lshl_add_u32 v34, s8, 10, v151
	ds_read_b128 v[34:37], v34
	s_cmp_gt_u32 s2, 30
	s_cbranch_scc1 .Lconv_b_zero_w3
	ds_read_b128 v[188:191], v181 offset:3072
	s_waitcnt lgkmcnt(0)
	v_lshlrev_b32_e32 v94, 16, v188
	v_lshlrev_b32_e32 v95, 16, v189
	v_and_b32_e32 v89, 0xffff0000, v189
	v_and_b32_e32 v88, 0xffff0000, v188
	v_lshlrev_b32_e32 v84, 16, v190
	v_lshlrev_b32_e32 v85, 16, v191
	v_and_b32_e32 v83, 0xffff0000, v191
	v_and_b32_e32 v82, 0xffff0000, v190
	s_branch .Lconv_b_294

; #define LAS __attribute__((address_space(3)))
; __device__ __forceinline__ void ph_convpool_fast(const Args& a, LAS unsigned char* lds) {
;     ...
;                 if (r < 31) unpack8(*(const LAS u32x4*)(lds + CW_OFF + r * 1024 + ch * 2), wq[u]);
;                 else {
; #pragma unroll
;                     for (int c = 0; c < 8; ++c) wq[u][c] = 0.f; }
.Lconv_b_zero_w1:
	v_mov_b32_e32 v92, 0
	v_mov_b32_e32 v93, 0
	v_mov_b32_e32 v98, 0
	v_mov_b32_e32 v99, 0
	v_mov_b32_e32 v106, 0
	v_mov_b32_e32 v107, 0
	v_mov_b32_e32 v120, 0
	v_mov_b32_e32 v121, 0
	s_branch .Lconv_b_299
.Lconv_b_zero_w2:
	v_mov_b32_e32 v86, 0
	v_mov_b32_e32 v87, 0
	v_mov_b32_e32 v90, 0
	v_mov_b32_e32 v91, 0
	v_mov_b32_e32 v96, 0
	v_mov_b32_e32 v97, 0
	v_mov_b32_e32 v102, 0
	v_mov_b32_e32 v103, 0
	s_branch .Lconv_b_301
.Lconv_b_zero_w3:
	v_mov_b32_e32 v82, 0
	v_mov_b32_e32 v83, 0
	v_mov_b32_e32 v84, 0
	v_mov_b32_e32 v85, 0
	v_mov_b32_e32 v88, 0
	v_mov_b32_e32 v89, 0
	v_mov_b32_e32 v94, 0
	v_mov_b32_e32 v95, 0
	s_branch .Lconv_b_294
